# MoE down epilogue: second row half's 8 gathered x loads issued with the first half's (one exposed load latency per down tile instead of two)
# speedup vs baseline: 1.0068x; 1.0038x over previous
.LBB0_1616:
	v_lshl_add_u32 v174, s55, 10, v189
	ds_read2_b32 v[128:129], v174 offset1:16
	ds_read2_b32 v[130:131], v174 offset0:32 offset1:48
	v_or_b32_e32 v172, s17, v190
	v_ashrrev_i32_e32 v173, 31, v172
	v_lshl_add_u64 v[178:179], v[172:173], 1, s[10:11]
	s_waitcnt lgkmcnt(0)
	v_ashrrev_i32_e32 v187, 31, v128
	v_mov_b32_e32 v186, v128
	v_ashrrev_i32_e32 v185, 31, v129
	v_mov_b32_e32 v184, v129
	v_lshlrev_b64 v[128:129], 10, v[186:187]
	v_cmp_lt_i64_e32 vcc, -1, v[186:187]
	v_cmp_lt_i64_e64 s[4:5], -1, v[184:185]
	v_ashrrev_i32_e32 v183, 31, v130
	v_cndmask_b32_e32 v129, 0, v129, vcc
	v_cndmask_b32_e32 v128, 0, v128, vcc
	v_lshl_add_u64 v[128:129], v[128:129], 1, v[178:179]
	global_load_dwordx4 v[156:159], v[128:129], off
	global_load_dwordx4 v[152:155], v[128:129], off offset:64
	v_lshlrev_b64 v[128:129], 10, v[184:185]
	v_cndmask_b32_e64 v129, 0, v129, s[4:5]
	v_cndmask_b32_e64 v128, 0, v128, s[4:5]
	v_mov_b32_e32 v182, v130
	v_lshl_add_u64 v[128:129], v[128:129], 1, v[178:179]
	global_load_dwordx4 v[148:151], v[128:129], off
	global_load_dwordx4 v[144:147], v[128:129], off offset:64
	v_lshlrev_b64 v[128:129], 10, v[182:183]
	v_cmp_lt_i64_e64 s[4:5], -1, v[182:183]
	v_ashrrev_i32_e32 v181, 31, v131
	v_mov_b32_e32 v180, v131
	v_cndmask_b32_e64 v129, 0, v129, s[4:5]
	v_cndmask_b32_e64 v128, 0, v128, s[4:5]
	v_lshl_add_u64 v[128:129], v[128:129], 1, v[178:179]
	global_load_dwordx4 v[140:143], v[128:129], off
	global_load_dwordx4 v[136:139], v[128:129], off offset:64
	v_lshlrev_b64 v[128:129], 10, v[180:181]
	v_cmp_lt_i64_e64 s[4:5], -1, v[180:181]
	s_nop 1
	v_cndmask_b32_e64 v129, 0, v129, s[4:5]
	v_cndmask_b32_e64 v128, 0, v128, s[4:5]
	v_lshl_add_u64 v[128:129], v[128:129], 1, v[178:179]
	global_load_dwordx4 v[132:135], v[128:129], off
	s_nop 0
	global_load_dwordx4 v[128:131], v[128:129], off offset:64
	ds_read2_b32 v[176:177], v174 offset0:128 offset1:144
	ds_read2_b32 v[174:175], v174 offset0:160 offset1:176
	s_waitcnt lgkmcnt(0)
	v_mov_b32_e32 v212, v176
	v_mov_b32_e32 v213, v209
	v_lshlrev_b64 v[212:213], 10, v[212:213]
	v_cmp_lt_i32_e64 s[98:99], -1, v176
	s_nop 1
	v_cndmask_b32_e64 v213, 0, v213, s[98:99]
	v_cndmask_b32_e64 v212, 0, v212, s[98:99]
	v_lshl_add_u64 v[212:213], v[212:213], 1, v[178:179]
	global_load_dwordx4 v[196:199], v[212:213], off
	global_load_dwordx4 v[200:203], v[212:213], off offset:64
	v_mov_b32_e32 v212, v177
	v_mov_b32_e32 v213, v209
	v_lshlrev_b64 v[212:213], 10, v[212:213]
	v_cmp_lt_i32_e64 s[98:99], -1, v177
	s_nop 1
	v_cndmask_b32_e64 v213, 0, v213, s[98:99]
	v_cndmask_b32_e64 v212, 0, v212, s[98:99]
	v_lshl_add_u64 v[212:213], v[212:213], 1, v[178:179]
	global_load_dwordx4 v[204:207], v[212:213], off
	global_load_dwordx4 v[232:235], v[212:213], off offset:64
	v_mov_b32_e32 v212, v174
	v_mov_b32_e32 v213, v209
	v_lshlrev_b64 v[212:213], 10, v[212:213]
	v_cmp_lt_i32_e64 s[98:99], -1, v174
	s_nop 1
	v_cndmask_b32_e64 v213, 0, v213, s[98:99]
	v_cndmask_b32_e64 v212, 0, v212, s[98:99]
	v_lshl_add_u64 v[212:213], v[212:213], 1, v[178:179]
	global_load_dwordx4 v[236:239], v[212:213], off
	global_load_dwordx4 v[240:243], v[212:213], off offset:64
	v_mov_b32_e32 v212, v175
	v_mov_b32_e32 v213, v209
	v_lshlrev_b64 v[212:213], 10, v[212:213]
	v_cmp_lt_i32_e64 s[98:99], -1, v175
	s_nop 1
	v_cndmask_b32_e64 v213, 0, v213, s[98:99]
	v_cndmask_b32_e64 v212, 0, v212, s[98:99]
	v_lshl_add_u64 v[212:213], v[212:213], 1, v[178:179]
	global_load_dwordx4 v[244:247], v[212:213], off
	global_load_dwordx4 v[216:219], v[212:213], off offset:64
	s_waitcnt vmcnt(0)
	s_and_saveexec_b64 s[4:5], vcc
	s_cbranch_execnz .LBB0_1629
	s_or_b64 exec, exec, s[4:5]
	v_cmp_lt_i32_e32 vcc, -1, v184
	s_and_saveexec_b64 s[4:5], vcc
	s_cbranch_execnz .LBB0_1630

.LBB0_1621:
	s_or_b64 exec, exec, s[4:5]
	s_waitcnt lgkmcnt(0)
	v_mov_b32_e32 v208, v176
	v_lshlrev_b64 v[64:65], 10, v[208:209]
	v_cmp_lt_i32_e32 vcc, -1, v176
	v_mov_b32_e32 v100, v177
	v_mov_b32_e32 v101, v209
	v_cndmask_b32_e32 v65, 0, v65, vcc
	v_cndmask_b32_e32 v64, 0, v64, vcc
	v_lshl_add_u64 v[64:65], v[64:65], 1, v[178:179]
	v_lshlrev_b64 v[64:65], 10, v[100:101]
	v_cmp_lt_i32_e64 s[4:5], -1, v177
	v_mov_b32_e32 v98, v174
	v_mov_b32_e32 v99, v209
	v_cndmask_b32_e64 v65, 0, v65, s[4:5]
	v_cndmask_b32_e64 v64, 0, v64, s[4:5]
	v_lshl_add_u64 v[64:65], v[64:65], 1, v[178:179]
	v_lshlrev_b64 v[64:65], 10, v[98:99]
	v_cmp_lt_i32_e64 s[4:5], -1, v174
	v_mov_b32_e32 v96, v175
	v_mov_b32_e32 v97, v209
	v_cndmask_b32_e64 v65, 0, v65, s[4:5]
	v_cndmask_b32_e64 v64, 0, v64, s[4:5]
	v_lshl_add_u64 v[64:65], v[64:65], 1, v[178:179]
	v_lshlrev_b64 v[64:65], 10, v[96:97]
	v_cmp_lt_i32_e64 s[4:5], -1, v175
	s_nop 1
	v_cndmask_b32_e64 v65, 0, v65, s[4:5]
	v_cndmask_b32_e64 v64, 0, v64, s[4:5]
	v_lshl_add_u64 v[64:65], v[64:65], 1, v[178:179]
	s_nop 0
	v_mov_b64_e32 v[92:93], v[196:197]
	v_mov_b64_e32 v[94:95], v[198:199]
	v_mov_b64_e32 v[88:89], v[200:201]
	v_mov_b64_e32 v[90:91], v[202:203]
	v_mov_b64_e32 v[84:85], v[204:205]
	v_mov_b64_e32 v[86:87], v[206:207]
	v_mov_b64_e32 v[80:81], v[232:233]
	v_mov_b64_e32 v[82:83], v[234:235]
	v_mov_b64_e32 v[76:77], v[236:237]
	v_mov_b64_e32 v[78:79], v[238:239]
	v_mov_b64_e32 v[72:73], v[240:241]
	v_mov_b64_e32 v[74:75], v[242:243]
	v_mov_b64_e32 v[68:69], v[244:245]
	v_mov_b64_e32 v[70:71], v[246:247]
	v_mov_b64_e32 v[64:65], v[216:217]
	v_mov_b64_e32 v[66:67], v[218:219]
	s_and_saveexec_b64 s[4:5], vcc
	s_cbranch_execnz .LBB0_1632
	s_or_b64 exec, exec, s[4:5]
	v_cmp_lt_i32_e32 vcc, -1, v177
	s_and_saveexec_b64 s[4:5], vcc
	s_cbranch_execnz .LBB0_1633
